# speedup vs baseline: 1.0038x; 1.0038x over previous
.LBB4_36:
	s_or_b64 exec, exec, s[32:33]
	s_waitcnt lgkmcnt(0)
	s_barrier
	s_setprio 1
	ds_read_b128 v[18:21], v75 offset:8192
	ds_read_b128 v[22:25], v74
	ds_read_b128 v[26:29], v75 offset:9216
	s_add_i32 s23, s23, -1
	s_add_u32 s0, s0, 0x480
	s_addc_u32 s1, s1, 0
	s_waitcnt lgkmcnt(1)
	v_mfma_f32_16x16x32_f16 v[2:5], v[18:21], v[22:25], v[2:5]
	ds_read_b128 v[18:21], v75 offset:10240
	v_lshl_add_u64 v[72:73], v[72:73], 0, s[34:35]
	s_cmp_eq_u32 s23, 0
	s_waitcnt lgkmcnt(1)
	v_mfma_f32_16x16x32_f16 v[6:9], v[26:29], v[22:25], v[6:9]
	ds_read_b128 v[26:29], v75 offset:11264
	v_lshl_add_u64 v[76:77], v[76:77], 0, 64
	s_waitcnt lgkmcnt(1)
	v_mfma_f32_16x16x32_f16 v[10:13], v[18:21], v[22:25], v[10:13]
	s_waitcnt lgkmcnt(0)
	v_mfma_f32_16x16x32_f16 v[14:17], v[26:29], v[22:25], v[14:17]
	s_cbranch_scc1 .LBB4_41
